# speedup vs baseline: 1.0188x; 1.0050x over previous
_Z11main_kernelPKDv4_jPKfS3_PfPjS4_:
	s_and_b32 s4, s2, 7
	s_ashr_i32 s5, s2, 3
	s_bfe_u32 s3, s2, 0x20001
	s_lshl_b32 s2, s2, 5
	s_and_b32 s2, s2, 32
	s_load_dwordx8 s[16:23], s[0:1], 0x0
	s_add_i32 s2, s2, s5
	s_lshl_b32 s33, s2, 1
	s_lshl_b32 s8, s3, 7
	s_add_i32 s10, s33, s8
	s_mov_b32 s8, s10
	v_and_b32_e32 v194, 63, v0
	v_writelane_b32 v240, s8, 0
	s_mul_i32 s35, s5, 5
	s_mov_b32 s47, 0x20000
	s_mov_b32 s46, 0x400000
	s_waitcnt lgkmcnt(0)
	s_and_b32 s45, s17, 0xffff
	v_writelane_b32 v240, s9, 1
	s_lshl_b32 s8, s10, 13
	s_add_i32 s35, s35, s4
	s_mov_b32 s4, s16
	s_mov_b32 s5, s45
	s_mov_b32 s6, s46
	s_mov_b32 s7, s47
	v_lshlrev_b32_e32 v195, 4, v194
	s_or_b32 s9, s8, 0x400
	v_lshrrev_b32_e32 v1, 6, v0
	s_nop 0
	v_readfirstlane_b32 s97, v1
	s_lshl_b32 s98, s97, 11
	s_add_i32 s99, s8, s98
	buffer_load_dwordx4 v[34:37], v195, s[4:7], s99 offen
	buffer_load_dwordx4 v[38:41], v195, s[4:7], s99 offen offset:1024
	s_or_b32 s9, s8, 0x800
	v_lshrrev_b32_e32 v1, 6, v0
	s_or_b32 s10, s8, 0xc00
	s_or_b32 s9, s8, 0x1000
	s_and_b32 s12, s35, 15
	s_or_b32 s10, s8, 0x1400
	v_readfirstlane_b32 s52, v1
	s_lshl_b32 s53, s3, 20
	s_lshl_b32 s9, s12, 16
	s_lshl_b32 s95, s52, 13
	s_or_b32 s54, s9, s53
	s_add_i32 s54, s54, s95
	s_or_b32 s55, s54, 0x400
	buffer_load_dwordx4 v[18:21], v195, s[4:7], s54 offen
	buffer_load_dwordx4 v[22:25], v195, s[4:7], s55 offen
	s_or_b32 s9, s8, 0x1800
	s_or_b32 s10, s8, 0x1c00
	s_or_b32 s9, s8, 0x2000
	s_or_b32 s10, s8, 0x2400
	s_or_b32 s9, s8, 0x2800
	s_or_b32 vcc_lo, s54, 0x800
	s_or_b32 s10, s8, 0x2c00
	s_or_b32 vcc_hi, s54, 0xc00
	buffer_load_dwordx4 v[98:101], v195, s[4:7], vcc_lo offen
	buffer_load_dwordx4 v[102:105], v195, s[4:7], vcc_hi offen
	s_or_b32 s9, s8, 0x3000
	s_or_b32 s10, s8, 0x3400
	s_or_b32 s9, s8, 0x3800
	s_or_b32 s34, s54, 0x1000
	s_or_b32 s8, s8, 0x3c00
	s_or_b32 s41, s54, 0x1400
	buffer_load_dwordx4 v[106:109], v195, s[4:7], s34 offen
	buffer_load_dwordx4 v[110:113], v195, s[4:7], s41 offen
	s_lshl_b32 s8, s3, 12
	s_lshl_b32 s9, s2, 6
	v_and_b32_e32 v163, 31, v0
	s_add_i32 s9, s9, s8
	v_or_b32_e32 v2, s9, v163
	v_ashrrev_i32_e32 v3, 31, v2
	v_lshl_add_u64 v[2:3], v[2:3], 2, s[18:19]
	s_or_b32 s60, s54, 0x1800
	global_load_dword v198, v[2:3], off
	global_load_dword v199, v[2:3], off offset:128
	s_or_b32 s61, s54, 0x1c00
	buffer_load_dwordx4 v[114:117], v195, s[4:7], s60 offen
	buffer_load_dwordx4 v[118:121], v195, s[4:7], s61 offen
	s_lshl_b32 s2, s2, 20
	s_lshl_b32 s3, s3, 26
	v_bfe_u32 v196, v0, 5, 1
	s_lshl_b32 s13, s52, 7
	v_lshlrev_b32_e32 v197, 2, v163
	s_add_i32 s62, s2, s3
	s_brev_b32 s38, 8
	s_and_b32 s37, s21, 0xffff
	v_lshl_or_b32 v201, v196, 16, v197
	s_add_i32 s62, s62, s13
	s_mov_b32 s8, s20
	s_mov_b32 s9, s37
	s_mov_b32 s10, s38
	s_mov_b32 s11, s47
	v_lshl_or_b32 v26, s12, 10, v201
	s_add_i32 s70, s62, 0x40000
	s_add_i32 s78, s62, 0x80000
	s_add_i32 s86, s62, 0xc0000
	s_add_i32 s63, s62, 0x4000
	s_add_i32 s64, s62, 0x8000
	s_add_i32 s65, s62, 0xc000
	s_add_i32 s66, s62, 0x20000
	s_add_i32 s67, s62, 0x24000
	s_add_i32 s68, s62, 0x28000
	s_add_i32 s69, s62, 0x2c000
	buffer_load_dword v218, v26, s[8:11], s62 offen nt
	buffer_load_dword v220, v26, s[8:11], s63 offen nt
	buffer_load_dword v222, v26, s[8:11], s64 offen nt
	buffer_load_dword v225, v26, s[8:11], s65 offen nt
	buffer_load_dword v219, v26, s[8:11], s66 offen nt
	buffer_load_dword v221, v26, s[8:11], s67 offen nt
	buffer_load_dword v223, v26, s[8:11], s68 offen nt
	buffer_load_dword v226, v26, s[8:11], s69 offen nt
	s_add_i32 s71, s62, 0x44000
	s_add_i32 s72, s62, 0x48000
	s_add_i32 s73, s62, 0x4c000
	s_add_i32 s74, s62, 0x60000
	s_add_i32 s75, s62, 0x64000
	s_add_i32 s76, s62, 0x68000
	s_add_i32 s77, s62, 0x6c000
	buffer_load_dword v232, v26, s[8:11], s70 offen nt
	buffer_load_dword v233, v26, s[8:11], s71 offen nt
	buffer_load_dword v234, v26, s[8:11], s72 offen nt
	buffer_load_dword v235, v26, s[8:11], s73 offen nt
	buffer_load_dword v228, v26, s[8:11], s74 offen nt
	buffer_load_dword v229, v26, s[8:11], s75 offen nt
	buffer_load_dword v230, v26, s[8:11], s76 offen nt
	buffer_load_dword v231, v26, s[8:11], s77 offen nt
	s_add_i32 s79, s62, 0x84000
	s_add_i32 s80, s62, 0x88000
	s_add_i32 s81, s62, 0x8c000
	s_add_i32 s82, s62, 0xa0000
	s_add_i32 s83, s62, 0xa4000
	s_add_i32 s84, s62, 0xa8000
	s_add_i32 s85, s62, 0xac000
	buffer_load_dword v203, v26, s[8:11], s78 offen nt
	buffer_load_dword v205, v26, s[8:11], s79 offen nt
	buffer_load_dword v207, v26, s[8:11], s80 offen nt
	buffer_load_dword v210, v26, s[8:11], s81 offen nt
	buffer_load_dword v204, v26, s[8:11], s82 offen nt
	buffer_load_dword v206, v26, s[8:11], s83 offen nt
	buffer_load_dword v208, v26, s[8:11], s84 offen nt
	buffer_load_dword v211, v26, s[8:11], s85 offen nt
	s_add_i32 s87, s62, 0xc4000
	s_add_i32 s88, s62, 0xc8000
	s_add_i32 s89, s62, 0xcc000
	s_add_i32 s90, s62, 0xe0000
	s_add_i32 s91, s62, 0xe4000
	s_add_i32 s92, s62, 0xe8000
	s_add_i32 s93, s62, 0xec000
	buffer_load_dword v212, v26, s[8:11], s86 offen nt
	buffer_load_dword v213, v26, s[8:11], s87 offen nt
	buffer_load_dword v214, v26, s[8:11], s88 offen nt
	buffer_load_dword v215, v26, s[8:11], s89 offen nt
	buffer_load_dword v190, v26, s[8:11], s90 offen nt
	buffer_load_dword v192, v26, s[8:11], s91 offen nt
	buffer_load_dword v193, v26, s[8:11], s92 offen nt
	buffer_load_dword v202, v26, s[8:11], s93 offen nt
	s_waitcnt vmcnt(42)
	v_add_u32_e32 v2, s98, v195
	ds_write_b128 v2, v[34:37] offset:40960
	ds_write_b128 v2, v[38:41] offset:41984
	s_waitcnt lgkmcnt(0)
	s_barrier
	ds_read_b128 v[34:37], v195 offset:40960
	ds_read_b128 v[38:41], v195 offset:41984
	ds_read_b128 v[42:45], v195 offset:43008
	ds_read_b128 v[46:49], v195 offset:44032
	ds_read_b128 v[50:53], v195 offset:45056
	ds_read_b128 v[54:57], v195 offset:46080
	ds_read_b128 v[58:61], v195 offset:47104
	ds_read_b128 v[62:65], v195 offset:48128
	ds_read_b128 v[66:69], v195 offset:49152
	ds_read_b128 v[70:73], v195 offset:50176
	ds_read_b128 v[74:77], v195 offset:51200
	ds_read_b128 v[78:81], v195 offset:52224
	ds_read_b128 v[82:85], v195 offset:53248
	ds_read_b128 v[86:89], v195 offset:54272
	ds_read_b128 v[90:93], v195 offset:55296
	ds_read_b128 v[94:97], v195 offset:56320
	v_mov_b32_e32 v236, 0x7f7f7f7f
	s_load_dwordx4 s[0:3], s[0:1], 0x20
	s_mov_b32 s44, s16
	s_waitcnt vmcnt(40)
	s_waitcnt lgkmcnt(0)
	v_mfma_scale_f32_32x32x64_f8f6f4 v[2:17], v[34:41], v[18:25], 0, v236, v236 op_sel_hi:[0,0,0]
	v_lshlrev_b32_e32 v160, 2, v196
	s_mov_b32 s39, s47
	s_waitcnt lgkmcnt(0)
	v_writelane_b32 v240, s0, 2
	s_mov_b32 s94, 0
	v_mov_b32_e32 v162, 0
	v_writelane_b32 v240, s1, 3
	v_writelane_b32 v240, s2, 4
	v_writelane_b32 v240, s3, 5
	v_writelane_b32 v240, s16, 6
	s_mov_b32 s36, s20
	v_sub_u32_e32 v26, v163, v160
	v_writelane_b32 v240, s17, 7
	v_writelane_b32 v240, s18, 8
	v_writelane_b32 v240, s19, 9
	v_writelane_b32 v240, s20, 10
	s_waitcnt vmcnt(38)
	v_mfma_scale_f32_32x32x64_f8f6f4 v[2:17], v[42:49], v[98:105], v[2:17], v236, v236 op_sel_hi:[0,0,0]
	v_writelane_b32 v240, s21, 11
	v_writelane_b32 v240, s22, 12
	v_writelane_b32 v240, s23, 13
	s_waitcnt vmcnt(36)
	v_mfma_scale_f32_32x32x64_f8f6f4 v[2:17], v[50:57], v[106:113], v[2:17], v236, v236 op_sel_hi:[0,0,0]
	s_waitcnt vmcnt(32)
	v_mfma_scale_f32_32x32x64_f8f6f4 v[2:17], v[58:65], v[114:121], v[2:17], v236, v236 op_sel_hi:[0,0,0]
	s_lshl_b32 s0, s52, 12
	s_add_i32 s95, s95, s53
	s_or_b32 s40, s33, 1
	v_writelane_b32 v240, s0, 14
	v_lshl_or_b32 v200, v194, 2, s0
	v_cmp_eq_u32_e64 s[0:1], v163, v160
	v_cmp_eq_u32_e64 s[2:3], 1, v26
	v_cmp_eq_u32_e64 s[4:5], 2, v26
	v_cmp_eq_u32_e64 s[6:7], 3, v26
	v_cmp_eq_u32_e64 s[8:9], 8, v26
	v_cmp_eq_u32_e64 s[10:11], 9, v26
	v_cmp_eq_u32_e64 s[12:13], 10, v26
	v_cmp_eq_u32_e64 s[14:15], 11, v26
	v_cmp_eq_u32_e64 s[16:17], 16, v26
	v_cmp_eq_u32_e64 s[18:19], 17, v26
	v_cmp_eq_u32_e64 s[20:21], 18, v26
	v_cmp_eq_u32_e64 s[22:23], 19, v26
	v_cmp_eq_u32_e64 s[24:25], 24, v26
	v_cmp_eq_u32_e64 s[26:27], 25, v26
	v_cmp_eq_u32_e64 s[28:29], 26, v26
	v_cmp_eq_u32_e64 s[30:31], 27, v26
	s_mov_b32 s96, 0x3f4ccccd
	v_mov_b32_e32 v161, 0
	v_mov_b32_e32 v159, 0
	v_mov_b32_e32 v158, 0
	v_mov_b32_e32 v157, 0
	v_mov_b32_e32 v156, 0
	v_mov_b32_e32 v155, 0
	v_mov_b32_e32 v154, 0
	v_mov_b32_e32 v227, 0
	v_mov_b32_e32 v224, 0
	v_mov_b32_e32 v217, 0
	v_mov_b32_e32 v216, 0
	v_mov_b32_e32 v209, 0
	v_mov_b32_e32 v191, 0
	v_mov_b32_e32 v189, 0
	v_mov_b32_e32 v188, 0
	v_mov_b32_e32 v187, 0
	v_mov_b32_e32 v186, 0
	v_mov_b32_e32 v185, 0
	v_mov_b32_e32 v184, 0
	v_mov_b32_e32 v183, 0
	v_mov_b32_e32 v182, 0
	v_mov_b32_e32 v181, 0
	v_mov_b32_e32 v180, 0
	v_mov_b32_e32 v179, 0
	v_mov_b32_e32 v178, 0
	v_mov_b32_e32 v177, 0
	v_mov_b32_e32 v176, 0
	v_mov_b32_e32 v175, 0
	v_mov_b32_e32 v174, 0
	v_mov_b32_e32 v173, 0
	v_mov_b32_e32 v172, 0
	v_mov_b32_e32 v171, 0
	v_mov_b32_e32 v170, 0
	v_mov_b32_e32 v169, 0
	v_mov_b32_e32 v168, 0
	v_mov_b32_e32 v167, 0
	v_mov_b32_e32 v166, 0
	v_mov_b32_e32 v165, 0
	v_mov_b32_e32 v164, 0

	.amdhsa_kernel _Z11main_kernelPKDv4_jPKfS3_PfPjS4_
		.amdhsa_group_segment_fixed_size 57344
		.amdhsa_private_segment_fixed_size 0
		.amdhsa_kernarg_size 48
		.amdhsa_user_sgpr_count 2
		.amdhsa_user_sgpr_dispatch_ptr 0
		.amdhsa_user_sgpr_queue_ptr 0
		.amdhsa_user_sgpr_kernarg_segment_ptr 1
		.amdhsa_user_sgpr_dispatch_id 0
		.amdhsa_user_sgpr_kernarg_preload_length 0
		.amdhsa_user_sgpr_kernarg_preload_offset 0
		.amdhsa_user_sgpr_private_segment_size 0
		.amdhsa_uses_dynamic_stack 0
		.amdhsa_enable_private_segment 0
		.amdhsa_system_sgpr_workgroup_id_x 1
		.amdhsa_system_sgpr_workgroup_id_y 0
		.amdhsa_system_sgpr_workgroup_id_z 0
		.amdhsa_system_sgpr_workgroup_info 0
		.amdhsa_system_vgpr_workitem_id 0
		.amdhsa_next_free_vgpr 241
		.amdhsa_next_free_sgpr 100
		.amdhsa_accum_offset 244
		.amdhsa_reserve_vcc 1
		.amdhsa_float_round_mode_32 0
		.amdhsa_float_round_mode_16_64 0
		.amdhsa_float_denorm_mode_32 3
		.amdhsa_float_denorm_mode_16_64 3
		.amdhsa_dx10_clamp 1
		.amdhsa_ieee_mode 1
		.amdhsa_fp16_overflow 0
		.amdhsa_tg_split 0
		.amdhsa_exception_fp_ieee_invalid_op 0
		.amdhsa_exception_fp_denorm_src 0
		.amdhsa_exception_fp_ieee_div_zero 0
		.amdhsa_exception_fp_ieee_overflow 0
		.amdhsa_exception_fp_ieee_underflow 0
		.amdhsa_exception_fp_ieee_inexact 0
		.amdhsa_exception_int_div_zero 0
	.end_amdhsa_kernel

amdhsa.kernels:
  - .agpr_count:     0
    .args:
      - .actual_access:  read_only
        .address_space:  global
        .offset:         0
        .size:           8
        .value_kind:     global_buffer
      - .actual_access:  write_only
        .address_space:  global
        .offset:         8
        .size:           8
        .value_kind:     global_buffer
      - .actual_access:  write_only
        .address_space:  global
        .offset:         16
        .size:           8
        .value_kind:     global_buffer
      - .actual_access:  write_only
        .address_space:  global
        .offset:         24
        .size:           8
        .value_kind:     global_buffer
    .group_segment_fixed_size: 0
    .kernarg_segment_align: 8
    .kernarg_segment_size: 32
    .language:       OpenCL C
    .language_version:
      - 2
      - 0
    .max_flat_workgroup_size: 256
    .name:           _Z11prep_kernelPKfPjPfS1_
    .private_segment_fixed_size: 0
    .sgpr_count:     18
    .sgpr_spill_count: 0
    .symbol:         _Z11prep_kernelPKfPjPfS1_.kd
    .uniform_work_group_size: 1
    .uses_dynamic_stack: false
    .vgpr_count:     46
    .vgpr_spill_count: 0
    .wavefront_size: 64
  - .agpr_count:     0
    .args:
      - .actual_access:  read_only
        .address_space:  global
        .offset:         0
        .size:           8
        .value_kind:     global_buffer
      - .actual_access:  read_only
        .address_space:  global
        .offset:         8
        .size:           8
        .value_kind:     global_buffer
      - .actual_access:  read_only
        .address_space:  global
        .offset:         16
        .size:           8
        .value_kind:     global_buffer
      - .address_space:  global
        .offset:         24
        .size:           8
        .value_kind:     global_buffer
      - .address_space:  global
        .offset:         32
        .size:           8
        .value_kind:     global_buffer
      - .actual_access:  write_only
        .address_space:  global
        .offset:         40
        .size:           8
        .value_kind:     global_buffer
    .group_segment_fixed_size: 57344
    .kernarg_segment_align: 8
    .kernarg_segment_size: 48
    .language:       OpenCL C
    .language_version:
      - 2
      - 0
    .max_flat_workgroup_size: 512
    .name:           _Z11main_kernelPKDv4_jPKfS3_PfPjS4_
    .private_segment_fixed_size: 0
    .sgpr_count:     106
    .sgpr_spill_count: 15
    .symbol:         _Z11main_kernelPKDv4_jPKfS3_PfPjS4_.kd
    .uniform_work_group_size: 1
    .uses_dynamic_stack: false
    .vgpr_count:     241
    .vgpr_spill_count: 0
    .wavefront_size: 64
